# nca kernels: QK accumulator-init quads (column+row mask, 7 rows x 4 regs) fully precomputed in the load-wait shadow; row-first MFMAs take them as SrcC; 28 more VALU per wave out of the QK phase
# baseline (speedup 1.0000x reference)
.LBB1_14:
	s_or_b64 exec, exec, s[14:15]
	s_movk_i32 s62, 0x80
	v_lshrrev_b32_e32 v127, 8, v0
	v_or_b32_e32 v128, s20, v62
	v_mad_u32_u24 v129, v127, 7, 0
	v_add_u32_e32 v130, v128, v129
	v_sub_u32_e32 v129, v129, v1
	v_cmp_gt_u32_e64 s[58:59], 11, v129
	v_cmp_gt_u32_e64 s[60:61], s62, v130
	s_and_b64 s[44:45], s[58:59], s[60:61]
	v_mad_u32_u24 v129, v127, 7, 1
	v_add_u32_e32 v130, v128, v129
	v_sub_u32_e32 v129, v129, v1
	v_cmp_gt_u32_e64 s[58:59], 11, v129
	v_cmp_gt_u32_e64 s[60:61], s62, v130
	s_and_b64 s[46:47], s[58:59], s[60:61]
	v_mad_u32_u24 v129, v127, 7, 2
	v_add_u32_e32 v130, v128, v129
	v_sub_u32_e32 v129, v129, v1
	v_cmp_gt_u32_e64 s[58:59], 11, v129
	v_cmp_gt_u32_e64 s[60:61], s62, v130
	s_and_b64 s[48:49], s[58:59], s[60:61]
	v_mad_u32_u24 v129, v127, 7, 3
	v_add_u32_e32 v130, v128, v129
	v_sub_u32_e32 v129, v129, v1
	v_cmp_gt_u32_e64 s[58:59], 11, v129
	v_cmp_gt_u32_e64 s[60:61], s62, v130
	s_and_b64 s[50:51], s[58:59], s[60:61]
	v_mad_u32_u24 v129, v127, 7, 4
	v_add_u32_e32 v130, v128, v129
	v_sub_u32_e32 v129, v129, v1
	v_cmp_gt_u32_e64 s[58:59], 11, v129
	v_cmp_gt_u32_e64 s[60:61], s62, v130
	s_and_b64 s[52:53], s[58:59], s[60:61]
	v_mad_u32_u24 v129, v127, 7, 5
	v_add_u32_e32 v130, v128, v129
	v_sub_u32_e32 v129, v129, v1
	v_cmp_gt_u32_e64 s[58:59], 11, v129
	v_cmp_gt_u32_e64 s[60:61], s62, v130
	s_and_b64 s[54:55], s[58:59], s[60:61]
	v_mad_u32_u24 v129, v127, 7, 6
	v_add_u32_e32 v130, v128, v129
	v_sub_u32_e32 v129, v129, v1
	v_cmp_gt_u32_e64 s[58:59], 11, v129
	v_cmp_gt_u32_e64 s[60:61], s62, v130
	s_and_b64 s[56:57], s[58:59], s[60:61]
	v_bfe_u32 v131, v0, 4, 2
	v_lshlrev_b32_e32 v131, 2, v131
	v_or_b32_e32 v132, s21, v63
	v_mov_b32_e32 v133, 0xff800000
	v_or_b32_e32 v134, 0, v131
	v_add_u32_e32 v135, v132, v134
	v_sub_u32_e32 v136, v134, v61
	v_cmp_gt_u32_e64 s[58:59], 11, v136
	v_cmp_gt_u32_e64 s[60:61], s62, v135
	s_and_b64 s[58:59], s[58:59], s[60:61]
	v_cndmask_b32_e64 v137, v133, 0, s[58:59]
	v_or_b32_e32 v134, 1, v131
	v_add_u32_e32 v135, v132, v134
	v_sub_u32_e32 v136, v134, v61
	v_cmp_gt_u32_e64 s[58:59], 11, v136
	v_cmp_gt_u32_e64 s[60:61], s62, v135
	s_and_b64 s[58:59], s[58:59], s[60:61]
	v_cndmask_b32_e64 v138, v133, 0, s[58:59]
	v_or_b32_e32 v134, 2, v131
	v_add_u32_e32 v135, v132, v134
	v_sub_u32_e32 v136, v134, v61
	v_cmp_gt_u32_e64 s[58:59], 11, v136
	v_cmp_gt_u32_e64 s[60:61], s62, v135
	s_and_b64 s[58:59], s[58:59], s[60:61]
	v_cndmask_b32_e64 v139, v133, 0, s[58:59]
	v_or_b32_e32 v134, 3, v131
	v_add_u32_e32 v135, v132, v134
	v_sub_u32_e32 v136, v134, v61
	v_cmp_gt_u32_e64 s[58:59], 11, v136
	v_cmp_gt_u32_e64 s[60:61], s62, v135
	s_and_b64 s[58:59], s[58:59], s[60:61]
	v_cndmask_b32_e64 v140, v133, 0, s[58:59]
	v_cndmask_b32_e64 v144, v133, v137, s[44:45]
	v_cndmask_b32_e64 v145, v133, v138, s[44:45]
	v_cndmask_b32_e64 v146, v133, v139, s[44:45]
	v_cndmask_b32_e64 v147, v133, v140, s[44:45]
	v_cndmask_b32_e64 v148, v133, v137, s[46:47]
	v_cndmask_b32_e64 v149, v133, v138, s[46:47]
	v_cndmask_b32_e64 v150, v133, v139, s[46:47]
	v_cndmask_b32_e64 v151, v133, v140, s[46:47]
	v_cndmask_b32_e64 v152, v133, v137, s[48:49]
	v_cndmask_b32_e64 v153, v133, v138, s[48:49]
	v_cndmask_b32_e64 v154, v133, v139, s[48:49]
	v_cndmask_b32_e64 v155, v133, v140, s[48:49]
	v_cndmask_b32_e64 v156, v133, v137, s[50:51]
	v_cndmask_b32_e64 v157, v133, v138, s[50:51]
	v_cndmask_b32_e64 v158, v133, v139, s[50:51]
	v_cndmask_b32_e64 v159, v133, v140, s[50:51]
	v_cndmask_b32_e64 v160, v133, v137, s[52:53]
	v_cndmask_b32_e64 v161, v133, v138, s[52:53]
	v_cndmask_b32_e64 v162, v133, v139, s[52:53]
	v_cndmask_b32_e64 v163, v133, v140, s[52:53]
	v_cndmask_b32_e64 v164, v133, v137, s[54:55]
	v_cndmask_b32_e64 v165, v133, v138, s[54:55]
	v_cndmask_b32_e64 v166, v133, v139, s[54:55]
	v_cndmask_b32_e64 v167, v133, v140, s[54:55]
	v_cndmask_b32_e64 v168, v133, v137, s[56:57]
	v_cndmask_b32_e64 v169, v133, v138, s[56:57]
	v_cndmask_b32_e64 v170, v133, v139, s[56:57]
	v_cndmask_b32_e64 v171, v133, v140, s[56:57]
	v_mov_b32_e32 v52, 1
	v_lshlrev_b16_sdwa v52, v52, v65 dst_sel:DWORD dst_unused:UNUSED_PAD src0_sel:DWORD src1_sel:WORD_1
	v_mul_i32_i24_e32 v51, -9, v64
	v_add_u16_e32 v52, v52, v64
	v_mul_u32_u24_e32 v52, 0xa0, v52
	v_add_lshl_u32 v51, v51, v0, 4
	s_waitcnt vmcnt(9)
	v_cndmask_b32_e32 v29, 0, v29, vcc
	v_cndmask_b32_e32 v28, 0, v28, vcc
	v_cndmask_b32_e32 v27, 0, v27, vcc
	v_cndmask_b32_e32 v26, 0, v26, vcc
	v_add3_u32 v51, 0, v52, v51
	ds_write_b128 v51, v[26:29]
	v_lshlrev_b16_e32 v27, 1, v67
	v_mul_i32_i24_e32 v26, -9, v66
	v_add_u16_e32 v27, v27, v66
	v_mul_u32_u24_e32 v27, 0xa0, v27
	v_add_lshl_u32 v26, v26, v59, 4
	s_waitcnt vmcnt(8)
	v_cndmask_b32_e64 v33, 0, v33, s[2:3]
	v_cndmask_b32_e64 v32, 0, v32, s[2:3]
	v_cndmask_b32_e64 v31, 0, v31, s[2:3]
	v_cndmask_b32_e64 v30, 0, v30, s[2:3]
	v_add3_u32 v26, 0, v27, v26
	v_lshlrev_b16_e32 v27, 1, v69
	ds_write_b128 v26, v[30:33]
	v_mul_i32_i24_e32 v26, -9, v68
	v_add_u16_e32 v27, v27, v68
	v_mul_u32_u24_e32 v27, 0xa0, v27
	v_add_lshl_u32 v26, v26, v58, 4
	s_waitcnt vmcnt(7)
	v_cndmask_b32_e64 v37, 0, v37, s[4:5]
	v_cndmask_b32_e64 v36, 0, v36, s[4:5]
	v_cndmask_b32_e64 v35, 0, v35, s[4:5]
	v_cndmask_b32_e64 v34, 0, v34, s[4:5]
	v_add3_u32 v26, 0, v27, v26
	v_lshlrev_b16_e32 v27, 1, v72
	ds_write_b128 v26, v[34:37]
	v_mul_i32_i24_e32 v26, -9, v71
	v_add_u16_e32 v27, v27, v71
	v_mul_u32_u24_e32 v27, 0xa0, v27
	v_add_lshl_u32 v26, v26, v70, 4
	v_mul_u32_u24_e32 v28, 0xca5, v73
	s_waitcnt vmcnt(6)
	v_cndmask_b32_e64 v45, 0, v45, s[8:9]
	v_cndmask_b32_e64 v44, 0, v44, s[8:9]
	v_cndmask_b32_e64 v43, 0, v43, s[8:9]
	v_cndmask_b32_e64 v42, 0, v42, s[8:9]
	v_add3_u32 v26, 0, v27, v26
	v_lshrrev_b32_e32 v28, 18, v28
	ds_write_b128 v26, v[42:45]
	v_mul_u32_u24_e32 v27, 0x1c72, v73
	v_mov_b32_e32 v26, -9
	v_and_b32_e32 v28, 62, v28
	v_mul_i32_i24_sdwa v29, v27, v26 dst_sel:DWORD dst_unused:UNUSED_PAD src0_sel:WORD_1 src1_sel:DWORD
	v_add_u16_sdwa v27, v28, v27 dst_sel:DWORD dst_unused:UNUSED_PAD src0_sel:DWORD src1_sel:WORD_1
	v_mul_u32_u24_e32 v27, 0xa0, v27
	v_add_lshl_u32 v28, v29, v73, 4
	s_movk_i32 s2, 0x164
	v_bfe_u32 v50, v0, 4, 2
	s_waitcnt vmcnt(5)
	v_cndmask_b32_e64 v49, 0, v49, s[10:11]
	v_cndmask_b32_e64 v48, 0, v48, s[10:11]
	v_cndmask_b32_e64 v47, 0, v47, s[10:11]
	v_cndmask_b32_e64 v46, 0, v46, s[10:11]
	v_add3_u32 v27, 0, v27, v28
	v_cmp_gt_u32_e32 vcc, s2, v0
	ds_write_b128 v27, v[46:49]
	s_and_saveexec_b64 s[2:3], vcc
	s_cbranch_execz .LBB1_16
	v_mul_u32_u24_e32 v32, 0xca5, v74
	v_lshrrev_b32_e32 v32, 18, v32
	v_mul_u32_u24_e32 v27, 0x1c72, v74
	v_and_b32_e32 v32, 62, v32
	v_mul_i32_i24_sdwa v26, v27, v26 dst_sel:DWORD dst_unused:UNUSED_PAD src0_sel:WORD_1 src1_sel:DWORD
	v_add_u16_sdwa v27, v32, v27 dst_sel:DWORD dst_unused:UNUSED_PAD src0_sel:DWORD src1_sel:WORD_1
	v_mul_u32_u24_e32 v27, 0xa0, v27
	v_add_lshl_u32 v26, v26, v74, 4
	s_waitcnt vmcnt(4)
	v_cndmask_b32_e64 v31, 0, v41, s[6:7]
	v_cndmask_b32_e64 v30, 0, v40, s[6:7]
	v_cndmask_b32_e64 v29, 0, v39, s[6:7]
	v_cndmask_b32_e64 v28, 0, v38, s[6:7]
	v_add3_u32 v26, 0, v27, v26
	ds_write_b128 v26, v[28:31]
.LBB1_16:
	s_or_b64 exec, exec, s[2:3]
	s_movk_i32 s2, 0x168
	s_waitcnt vmcnt(4)
	v_and_b32_e32 v39, 63, v0
	v_and_b32_e32 v40, 15, v0
	v_lshlrev_b32_e32 v26, 3, v50
	v_cmp_gt_u32_e32 vcc, s2, v0
	s_and_saveexec_b64 s[2:3], vcc
	s_movk_i32 s4, 0xa0
	v_mad_u32_u24 v27, v0, s4, 0
	v_mov_b32_e32 v28, 0x3c00
	ds_write_b16 v27, v28 offset:144
	s_or_b64 exec, exec, s[2:3]
	v_lshlrev_b32_e32 v38, 2, v50
	v_or_b32_e32 v28, s21, v63
	v_add_u32_e32 v29, v28, v38
	v_sub_u32_e32 v30, v38, v61
	s_movk_i32 s7, 0x80
	v_cmp_gt_u32_e64 s[2:3], 11, v30
	v_cmp_gt_u32_e64 s[4:5], s7, v29
	v_or_b32_e32 v29, 1, v38
	s_and_b64 s[2:3], s[2:3], s[4:5]
	v_mov_b32_e32 v111, 0xff800000
	v_add_u32_e32 v30, v28, v29
	v_sub_u32_e32 v29, v29, v61
	v_cndmask_b32_e64 v112, v111, 0, s[2:3]
	v_cmp_gt_u32_e64 s[2:3], 11, v29
	v_cmp_gt_u32_e64 s[4:5], s7, v30
	v_or_b32_e32 v29, 2, v38
	v_lshrrev_b32_e32 v110, 8, v0
	s_and_b64 s[2:3], s[2:3], s[4:5]
	v_add_u32_e32 v30, v28, v29
	v_sub_u32_e32 v29, v29, v61
	v_cndmask_b32_e64 v113, v111, 0, s[2:3]
	v_cmp_gt_u32_e64 s[2:3], 11, v29
	v_or_b32_e32 v29, 3, v38
	v_mad_u32_u24 v41, v110, 7, v62
	v_cmp_gt_u32_e64 s[4:5], s7, v30
	v_add_u32_e32 v28, v28, v29
	v_mad_u32_u24 v98, v41, 20, v63
	s_and_b64 s[2:3], s[2:3], s[4:5]
	v_cmp_gt_u32_e64 s[4:5], s7, v28
	v_add_u32_e32 v28, v98, v40
	s_movk_i32 s6, 0xa0
	v_mul_lo_u32 v28, v28, s6
	v_add_u32_e32 v99, 0, v28
	v_mul_u32_u24_e32 v27, 7, v110
	v_sub_u32_e32 v29, v29, v61
	v_lshl_add_u32 v94, v26, 1, v99
	s_waitcnt lgkmcnt(0)
	s_barrier
	v_cndmask_b32_e64 v114, v111, 0, s[2:3]
	v_cmp_gt_u32_e64 s[2:3], 11, v29
	ds_read_b128 v[26:29], v94
	s_and_b64 s[2:3], s[2:3], s[4:5]
	ds_read_b128 v[34:37], v94 offset:64
	v_cndmask_b32_e64 v115, v111, 0, s[2:3]
	v_cmp_gt_u32_e32 vcc, 16, v39
	v_add_u32_e32 v98, v98, v38
	s_waitcnt lgkmcnt(1)
	v_mfma_f32_16x16x32_f16 v[30:33], v[26:29], v[10:13], v[144:147]
	ds_read_b128 v[42:45], v99 offset:128
	ds_read_b128 v[46:49], v94 offset:3200
	v_cndmask_b32_e32 v29, 0, v25, vcc
	s_waitcnt lgkmcnt(2)
	v_mfma_f32_16x16x32_f16 v[30:33], v[34:37], v[2:5], v[30:33]
	v_cndmask_b32_e32 v28, 0, v24, vcc
	v_cndmask_b32_e32 v27, 0, v23, vcc
	v_cndmask_b32_e32 v26, 0, v22, vcc
	ds_read_b128 v[34:37], v94 offset:3264
	ds_read_b128 v[50:53], v99 offset:3328
	s_waitcnt lgkmcnt(3)
	v_mfma_f32_16x16x32_f16 v[22:25], v[42:45], v[26:29], v[30:33]
	ds_read_b128 v[42:45], v94 offset:6400
	ds_read_b128 v[62:65], v94 offset:6464
	v_or_b32_e32 v98, v98, v1
	v_mul_lo_u32 v98, v98, s6
	v_lshlrev_b32_e32 v61, 3, v61
	s_waitcnt lgkmcnt(4)
	v_mfma_f32_16x16x32_f16 v[30:33], v[46:49], v[10:13], v[148:151]
	ds_read_b128 v[46:49], v99 offset:6528
	ds_read_b128 v[66:69], v94 offset:9600
	v_add3_u32 v61, 0, v98, v61
	s_waitcnt lgkmcnt(5)
	v_mfma_f32_16x16x32_f16 v[30:33], v[34:37], v[2:5], v[30:33]
	ds_read_b128 v[70:73], v94 offset:9664
	ds_read_b128 v[74:77], v99 offset:9728
	s_waitcnt lgkmcnt(6)
	v_mfma_f32_16x16x32_f16 v[30:33], v[50:53], v[26:29], v[30:33]
	ds_read_b128 v[50:53], v94 offset:12800
	ds_read_b128 v[78:81], v94 offset:12864
	s_waitcnt vmcnt(3)
	v_cvt_pk_f16_f32 v21, v20, v21
	s_waitcnt lgkmcnt(7)
	v_mfma_f32_16x16x32_f16 v[34:37], v[42:45], v[10:13], v[152:155]
	ds_read_b128 v[42:45], v99 offset:12928
	ds_read_b128 v[82:85], v94 offset:16000
	v_cvt_pk_f16_f32 v20, v18, v19
	s_waitcnt lgkmcnt(8)
	v_mfma_f32_16x16x32_f16 v[34:37], v[62:65], v[2:5], v[34:37]
	ds_read_b128 v[62:65], v94 offset:16064
	ds_read_b128 v[86:89], v99 offset:16128
	v_mul_u32_u24_e32 v18, 0xa0, v60
	s_waitcnt lgkmcnt(9)
	v_mfma_f32_16x16x32_f16 v[34:37], v[46:49], v[26:29], v[34:37]
	ds_read_b128 v[90:93], v94 offset:19200
	ds_read_b128 v[94:97], v94 offset:19264
	s_waitcnt lgkmcnt(10)
	v_mfma_f32_16x16x32_f16 v[46:49], v[66:69], v[10:13], v[156:159]
	ds_read_b128 v[66:69], v99 offset:19328
	ds_read_b64_tr_b16 v[100:101], v61 offset:3200
	v_lshlrev_b32_e32 v19, 1, v56
	s_waitcnt lgkmcnt(11)
	v_mfma_f32_16x16x32_f16 v[46:49], v[70:73], v[2:5], v[46:49]
	ds_read_b64_tr_b16 v[98:99], v61
	ds_read_b64_tr_b16 v[70:71], v61 offset:32
	s_waitcnt lgkmcnt(12)
	v_mfma_f32_16x16x32_f16 v[46:49], v[74:77], v[26:29], v[46:49]
	ds_read_b64_tr_b16 v[72:73], v61 offset:3232
	ds_read_b64_tr_b16 v[102:103], v61 offset:64
	s_waitcnt lgkmcnt(13)
	v_mfma_f32_16x16x32_f16 v[50:53], v[50:53], v[10:13], v[160:163]
	ds_read_b64_tr_b16 v[104:105], v61 offset:3264
	v_add3_u32 v18, 0, v18, v19
	s_movk_i32 s4, 0xe39
	ds_read_b64_tr_b16 v[74:75], v61 offset:96
	s_waitcnt lgkmcnt(14)
	v_mfma_f32_16x16x32_f16 v[50:53], v[78:81], v[2:5], v[50:53]
	ds_read_b64_tr_b16 v[76:77], v61 offset:3296
	ds_read_b64_tr_b16 v[78:79], v61 offset:128
	s_movk_i32 s5, 0xffee
	s_waitcnt lgkmcnt(14)
	v_mfma_f32_16x16x32_f16 v[42:45], v[42:45], v[26:29], v[50:53]
	ds_read_b64_tr_b16 v[80:81], v61 offset:3328
	ds_read_b64_tr_b16 v[106:107], v61 offset:6400
	s_waitcnt vmcnt(2)
	v_cvt_pk_f16_f32 v17, v16, v17
	v_cvt_pk_f16_f32 v16, v14, v15
	s_nop 0
	v_mfma_f32_16x16x32_f16 v[50:53], v[82:85], v[10:13], v[164:167]
	ds_read_b64_tr_b16 v[108:109], v61 offset:9600
	ds_read_b64_tr_b16 v[82:83], v61 offset:6432
	s_waitcnt lgkmcnt(14)
	v_mfma_f32_16x16x32_f16 v[50:53], v[62:65], v[2:5], v[50:53]
	ds_read_b64_tr_b16 v[84:85], v61 offset:9632
	ds_read_b64_tr_b16 v[62:63], v61 offset:6464
	v_mfma_f32_16x16x32_f16 v[50:53], v[86:89], v[26:29], v[50:53]
	ds_read_b64_tr_b16 v[64:65], v61 offset:9664
	ds_read_b64_tr_b16 v[110:111], v61 offset:6496
	v_mfma_f32_16x16x32_f16 v[10:13], v[90:93], v[10:13], v[168:171]
	s_mov_b32 s2, 0xff800000
	ds_read_b64_tr_b16 v[112:113], v61 offset:9696
	s_nop 0
	ds_read_b64_tr_b16 v[86:87], v61 offset:6528
	v_mfma_f32_16x16x32_f16 v[2:5], v[94:97], v[2:5], v[10:13]
	ds_read_b64_tr_b16 v[88:89], v61 offset:9728
	s_nop 1
	v_max3_f32 v12, v22, s2, v23
	v_max3_f32 v12, v12, v24, v25
	v_max3_f32 v12, v12, v30, v31
	v_max3_f32 v12, v12, v32, v33
	v_max3_f32 v12, v12, v34, v35
	v_max3_f32 v12, v12, v36, v37
	v_max3_f32 v12, v12, v46, v47
	v_max3_f32 v12, v12, v48, v49
	v_mbcnt_lo_u32_b32 v13, -1, 0
	ds_read_b64_tr_b16 v[10:11], v61 offset:12800
	s_waitcnt lgkmcnt(14)
	v_mfma_f32_16x16x32_f16 v[2:5], v[66:69], v[26:29], v[2:5]
	v_max3_f32 v12, v12, v42, v43
	v_mbcnt_hi_u32_b32 v13, -1, v13
	v_max3_f32 v12, v12, v44, v45
	v_and_b32_e32 v27, 64, v13
	v_max3_f32 v12, v12, v50, v51
	v_xor_b32_e32 v26, 16, v13
	v_add_u32_e32 v27, 64, v27
	v_max3_f32 v12, v12, v52, v53
	v_cmp_lt_i32_e32 vcc, v26, v27
	v_max3_f32 v12, v12, v2, v3
	v_max3_f32 v12, v12, v4, v5
	v_mov_b32_e32 v26, v12
	s_load_dwordx2 s[2:3], s[0:1], 0x20
	s_movk_i32 s0, 0x510
	v_permlane16_swap_b32_e32 v12, v26
	v_cmp_gt_u32_e32 vcc, 11, v41
	v_mov_b32_e32 v41, 0xc80
	v_max_f32_e32 v12, v12, v26
	v_mov_b32_e32 v13, v12
	s_nop 1
	v_permlane32_swap_b32_e32 v12, v13
	s_waitcnt lgkmcnt(0)
	s_nop 0
	v_max_f32_e32 v26, v12, v13
	v_sub_f32_e32 v29, v34, v26
	v_exp_f32_e32 v92, v29
	v_sub_f32_e32 v29, v35, v26
	v_exp_f32_e32 v93, v29
	v_sub_f32_e32 v29, v36, v26
	v_exp_f32_e32 v36, v29
	v_sub_f32_e32 v29, v37, v26
	v_exp_f32_e32 v37, v29
	v_sub_f32_e32 v29, v46, v26
	v_exp_f32_e32 v94, v29
	v_sub_f32_e32 v29, v47, v26
	v_exp_f32_e32 v95, v29
	v_sub_f32_e32 v29, v48, v26
	v_sub_f32_e32 v13, v23, v26
	v_sub_f32_e32 v23, v25, v26
	v_sub_f32_e32 v25, v31, v26
	v_exp_f32_e32 v96, v29
	v_sub_f32_e32 v29, v49, v26
	v_sub_f32_e32 v12, v22, v26
	v_sub_f32_e32 v22, v24, v26
	v_sub_f32_e32 v24, v30, v26
	v_exp_f32_e32 v27, v25
	v_sub_f32_e32 v25, v32, v26
	v_sub_f32_e32 v28, v33, v26
	v_exp_f32_e32 v97, v29
	v_sub_f32_e32 v29, v42, v26
	v_exp_f32_e32 v12, v12
	v_exp_f32_e32 v13, v13
	v_exp_f32_e32 v22, v22
	v_exp_f32_e32 v23, v23
	v_exp_f32_e32 v24, v24
	v_exp_f32_e32 v25, v25
	v_exp_f32_e32 v28, v28
	v_exp_f32_e32 v114, v29
	v_sub_f32_e32 v29, v43, v26
	v_exp_f32_e32 v115, v29
	v_sub_f32_e32 v29, v44, v26
	v_exp_f32_e32 v116, v29
	v_sub_f32_e32 v29, v45, v26
	v_exp_f32_e32 v117, v29
	v_sub_f32_e32 v29, v50, v26
	v_exp_f32_e32 v118, v29
	v_sub_f32_e32 v29, v51, v26
	v_cvt_pk_f16_f32 v25, v25, v28
	v_cvt_pk_f16_f32 v24, v24, v27
	v_cvt_pk_f16_f32 v23, v22, v23
	v_cvt_pk_f16_f32 v22, v12, v13
	v_exp_f32_e32 v119, v29
	v_cndmask_b32_e32 v41, 0, v41, vcc
	v_mfma_f32_16x16x32_f16 v[28:31], v[98:101], v[22:25], 0
	ds_read_b64_tr_b16 v[12:13], v61 offset:16000
	ds_read_b64_tr_b16 v[32:33], v61 offset:12832
	v_sub_f32_e32 v27, v52, v26
	v_mfma_f32_16x16x32_f16 v[42:45], v[70:73], v[22:25], 0
	ds_read_b64_tr_b16 v[34:35], v61 offset:16032
	ds_read_b64_tr_b16 v[46:47], v61 offset:12864
	v_exp_f32_e32 v27, v27
	v_mfma_f32_16x16x32_f16 v[66:69], v[102:105], v[22:25], 0
	ds_read_b64_tr_b16 v[48:49], v61 offset:16064
	ds_read_b64_tr_b16 v[70:71], v61 offset:12896
	v_sub_f32_e32 v2, v2, v26
	v_mfma_f32_16x16x32_f16 v[74:77], v[74:77], v[22:25], 0
	ds_read_b64_tr_b16 v[72:73], v61 offset:16096
	ds_read_b64_tr_b16 v[90:91], v61 offset:12928
	v_cmp_gt_u32_e32 vcc, s0, v58
	v_mfma_f32_16x16x32_f16 v[22:25], v[78:81], v[22:25], 0
	v_cvt_pk_f16_f32 v78, v92, v93
	ds_read_b64_tr_b16 v[92:93], v61 offset:16128
	v_cvt_pk_f16_f32 v81, v96, v97
	v_cvt_pk_f16_f32 v80, v94, v95
	v_cvt_pk_f16_f32 v79, v36, v37
	v_add_u32_e32 v36, v61, v41
	v_sub_f32_e32 v37, v53, v26
	ds_read_b64_tr_b16 v[94:95], v61 offset:19200
	v_mfma_f32_16x16x32_f16 v[28:31], v[106:109], v[78:81], v[28:31]
	ds_read_b64_tr_b16 v[96:97], v36 offset:19200
	ds_read_b64_tr_b16 v[100:101], v36 offset:19232
	v_exp_f32_e32 v37, v37
	v_mfma_f32_16x16x32_f16 v[42:45], v[82:85], v[78:81], v[42:45]
	ds_read_b64_tr_b16 v[98:99], v61 offset:19232
	ds_read_b64_tr_b16 v[50:51], v61 offset:19264
	v_mfma_f32_16x16x32_f16 v[62:65], v[62:65], v[78:81], v[66:69]
	ds_read_b64_tr_b16 v[52:53], v36 offset:19264
	s_nop 1
	ds_read_b64_tr_b16 v[66:67], v61 offset:19296
	v_mfma_f32_16x16x32_f16 v[74:77], v[110:113], v[78:81], v[74:77]
	ds_read_b64_tr_b16 v[68:69], v36 offset:19296
	ds_read_b64_tr_b16 v[82:83], v61 offset:19328
	v_mfma_f32_16x16x32_f16 v[22:25], v[86:89], v[78:81], v[22:25]
	ds_read_b64_tr_b16 v[84:85], v36 offset:19328
	ds_write_b64 v18, v[20:21] offset:57600
	v_mul_u32_u24_sdwa v18, v59, s4 dst_sel:DWORD dst_unused:UNUSED_PAD src0_sel:WORD_0 src1_sel:DWORD
	v_mul_i32_i24_sdwa v19, v18, s5 dst_sel:DWORD dst_unused:UNUSED_PAD src0_sel:WORD_1 src1_sel:DWORD
	v_mul_u32_u24_sdwa v14, v18, s6 dst_sel:DWORD dst_unused:UNUSED_PAD src0_sel:WORD_1 src1_sel:DWORD
	v_add_lshl_u32 v15, v19, v59, 3
	v_exp_f32_e32 v18, v2
	v_sub_f32_e32 v19, v3, v26
	v_sub_f32_e32 v2, v4, v26
	v_sub_f32_e32 v21, v5, v26
	v_cvt_pk_f16_f32 v81, v27, v37
	v_cvt_pk_f16_f32 v80, v118, v119
	v_cvt_pk_f16_f32 v79, v116, v117
	v_cvt_pk_f16_f32 v78, v114, v115
	v_add3_u32 v14, 0, v14, v15
	v_exp_f32_e32 v20, v2
	v_exp_f32_e32 v21, v21
	v_exp_f32_e32 v19, v19
	s_waitcnt lgkmcnt(14)
	v_mfma_f32_16x16x32_f16 v[10:13], v[10:13], v[78:81], v[28:31]
	ds_write_b64 v14, v[16:17] offset:57600
	v_mfma_f32_16x16x32_f16 v[14:17], v[32:35], v[78:81], v[42:45]
	v_mfma_f32_16x16x32_f16 v[28:31], v[46:49], v[78:81], v[62:65]
	s_nop 1
	v_mov_b32_e32 v44, 0
	v_cvt_pk_f16_f32 v43, v20, v21
	v_cvt_pk_f16_f32 v42, v18, v19
	s_waitcnt lgkmcnt(14)
	v_mfma_f32_16x16x32_f16 v[2:5], v[70:73], v[78:81], v[74:77]
	v_mov_b32_e32 v45, v44
	s_waitcnt lgkmcnt(12)
	v_mfma_f32_16x16x32_f16 v[32:35], v[90:93], v[78:81], v[22:25]
	s_waitcnt lgkmcnt(10)
	v_mfma_f32_16x16x32_f16 v[22:25], v[94:97], v[42:45], v[10:13]
	s_waitcnt lgkmcnt(8)
	v_mfma_f32_16x16x32_f16 v[18:21], v[98:101], v[42:45], v[14:17]
	s_waitcnt lgkmcnt(6)
	v_mfma_f32_16x16x32_f16 v[14:17], v[50:53], v[42:45], v[28:31]
	s_waitcnt lgkmcnt(4)
	v_mfma_f32_16x16x32_f16 v[10:13], v[66:69], v[42:45], v[2:5]
	s_waitcnt lgkmcnt(2)
	v_mfma_f32_16x16x32_f16 v[2:5], v[82:85], v[42:45], v[32:35]
	s_and_saveexec_b64 s[0:1], vcc
	s_cbranch_execz .LBB1_20
	v_mul_u32_u24_sdwa v27, v58, s4 dst_sel:DWORD dst_unused:UNUSED_PAD src0_sel:WORD_0 src1_sel:DWORD
	v_mul_i32_i24_sdwa v28, v27, s5 dst_sel:DWORD dst_unused:UNUSED_PAD src0_sel:WORD_1 src1_sel:DWORD
	s_waitcnt vmcnt(1)
	v_cvt_pk_f16_f32 v9, v8, v9
	v_cvt_pk_f16_f32 v8, v6, v7
	v_mul_u32_u24_sdwa v6, v27, s6 dst_sel:DWORD dst_unused:UNUSED_PAD src0_sel:WORD_1 src1_sel:DWORD
	v_add_lshl_u32 v7, v28, v58, 3
	v_add3_u32 v6, 0, v6, v7
	ds_write_b64 v6, v[8:9] offset:57600

	.amdhsa_kernel _Z5k_ncaILi0EEvPKDF16_S1_PKfS3_PDF16_S3_S3_S3_S3_Pf
		.amdhsa_group_segment_fixed_size 0
		.amdhsa_private_segment_fixed_size 0
		.amdhsa_kernarg_size 80
		.amdhsa_user_sgpr_count 2
		.amdhsa_user_sgpr_dispatch_ptr 0
		.amdhsa_user_sgpr_queue_ptr 0
		.amdhsa_user_sgpr_kernarg_segment_ptr 1
		.amdhsa_user_sgpr_dispatch_id 0
		.amdhsa_user_sgpr_kernarg_preload_length 0
		.amdhsa_user_sgpr_kernarg_preload_offset 0
		.amdhsa_user_sgpr_private_segment_size 0
		.amdhsa_uses_dynamic_stack 0
		.amdhsa_enable_private_segment 0
		.amdhsa_system_sgpr_workgroup_id_x 1
		.amdhsa_system_sgpr_workgroup_id_y 0
		.amdhsa_system_sgpr_workgroup_id_z 0
		.amdhsa_system_sgpr_workgroup_info 0
		.amdhsa_system_vgpr_workitem_id 0
		.amdhsa_next_free_vgpr 176
		.amdhsa_next_free_sgpr 96
		.amdhsa_accum_offset 176
		.amdhsa_reserve_vcc 1
		.amdhsa_float_round_mode_32 0
		.amdhsa_float_round_mode_16_64 0
		.amdhsa_float_denorm_mode_32 3
		.amdhsa_float_denorm_mode_16_64 3
		.amdhsa_dx10_clamp 1
		.amdhsa_ieee_mode 1
		.amdhsa_fp16_overflow 0
		.amdhsa_tg_split 0
		.amdhsa_exception_fp_ieee_invalid_op 0
		.amdhsa_exception_fp_denorm_src 0
		.amdhsa_exception_fp_ieee_div_zero 0
		.amdhsa_exception_fp_ieee_overflow 0
		.amdhsa_exception_fp_ieee_underflow 0
		.amdhsa_exception_fp_ieee_inexact 0
		.amdhsa_exception_int_div_zero 0
	.end_amdhsa_kernel

.LBB2_14:
	s_or_b64 exec, exec, s[14:15]
	s_movk_i32 s62, 0x80
	v_lshrrev_b32_e32 v144, 8, v0
	v_or_b32_e32 v145, s29, v76
	v_mad_u32_u24 v146, v144, 7, 0
	v_add_u32_e32 v147, v145, v146
	v_sub_u32_e32 v146, v146, v60
	v_cmp_gt_u32_e64 s[58:59], 11, v146
	v_cmp_gt_u32_e64 s[60:61], s62, v147
	s_and_b64 s[44:45], s[58:59], s[60:61]
	v_mad_u32_u24 v146, v144, 7, 1
	v_add_u32_e32 v147, v145, v146
	v_sub_u32_e32 v146, v146, v60
	v_cmp_gt_u32_e64 s[58:59], 11, v146
	v_cmp_gt_u32_e64 s[60:61], s62, v147
	s_and_b64 s[46:47], s[58:59], s[60:61]
	v_mad_u32_u24 v146, v144, 7, 2
	v_add_u32_e32 v147, v145, v146
	v_sub_u32_e32 v146, v146, v60
	v_cmp_gt_u32_e64 s[58:59], 11, v146
	v_cmp_gt_u32_e64 s[60:61], s62, v147
	s_and_b64 s[48:49], s[58:59], s[60:61]
	v_mad_u32_u24 v146, v144, 7, 3
	v_add_u32_e32 v147, v145, v146
	v_sub_u32_e32 v146, v146, v60
	v_cmp_gt_u32_e64 s[58:59], 11, v146
	v_cmp_gt_u32_e64 s[60:61], s62, v147
	s_and_b64 s[50:51], s[58:59], s[60:61]
	v_mad_u32_u24 v146, v144, 7, 4
	v_add_u32_e32 v147, v145, v146
	v_sub_u32_e32 v146, v146, v60
	v_cmp_gt_u32_e64 s[58:59], 11, v146
	v_cmp_gt_u32_e64 s[60:61], s62, v147
	s_and_b64 s[52:53], s[58:59], s[60:61]
	v_mad_u32_u24 v146, v144, 7, 5
	v_add_u32_e32 v147, v145, v146
	v_sub_u32_e32 v146, v146, v60
	v_cmp_gt_u32_e64 s[58:59], 11, v146
	v_cmp_gt_u32_e64 s[60:61], s62, v147
	s_and_b64 s[54:55], s[58:59], s[60:61]
	v_mad_u32_u24 v146, v144, 7, 6
	v_add_u32_e32 v147, v145, v146
	v_sub_u32_e32 v146, v146, v60
	v_cmp_gt_u32_e64 s[58:59], 11, v146
	v_cmp_gt_u32_e64 s[60:61], s62, v147
	s_and_b64 s[56:57], s[58:59], s[60:61]
	v_bfe_u32 v148, v0, 4, 2
	v_lshlrev_b32_e32 v148, 2, v148
	v_or_b32_e32 v149, s30, v57
	v_mov_b32_e32 v150, 0xff800000
	v_or_b32_e32 v151, 0, v148
	v_add_u32_e32 v152, v149, v151
	v_sub_u32_e32 v153, v151, v1
	v_cmp_gt_u32_e64 s[58:59], 11, v153
	v_cmp_gt_u32_e64 s[60:61], s62, v152
	s_and_b64 s[58:59], s[58:59], s[60:61]
	v_cndmask_b32_e64 v154, v150, 0, s[58:59]
	v_or_b32_e32 v151, 1, v148
	v_add_u32_e32 v152, v149, v151
	v_sub_u32_e32 v153, v151, v1
	v_cmp_gt_u32_e64 s[58:59], 11, v153
	v_cmp_gt_u32_e64 s[60:61], s62, v152
	s_and_b64 s[58:59], s[58:59], s[60:61]
	v_cndmask_b32_e64 v155, v150, 0, s[58:59]
	v_or_b32_e32 v151, 2, v148
	v_add_u32_e32 v152, v149, v151
	v_sub_u32_e32 v153, v151, v1
	v_cmp_gt_u32_e64 s[58:59], 11, v153
	v_cmp_gt_u32_e64 s[60:61], s62, v152
	s_and_b64 s[58:59], s[58:59], s[60:61]
	v_cndmask_b32_e64 v156, v150, 0, s[58:59]
	v_or_b32_e32 v151, 3, v148
	v_add_u32_e32 v152, v149, v151
	v_sub_u32_e32 v153, v151, v1
	v_cmp_gt_u32_e64 s[58:59], 11, v153
	v_cmp_gt_u32_e64 s[60:61], s62, v152
	s_and_b64 s[58:59], s[58:59], s[60:61]
	v_cndmask_b32_e64 v157, v150, 0, s[58:59]
	v_cndmask_b32_e64 v160, v150, v154, s[44:45]
	v_cndmask_b32_e64 v161, v150, v155, s[44:45]
	v_cndmask_b32_e64 v162, v150, v156, s[44:45]
	v_cndmask_b32_e64 v163, v150, v157, s[44:45]
	v_cndmask_b32_e64 v164, v150, v154, s[46:47]
	v_cndmask_b32_e64 v165, v150, v155, s[46:47]
	v_cndmask_b32_e64 v166, v150, v156, s[46:47]
	v_cndmask_b32_e64 v167, v150, v157, s[46:47]
	v_cndmask_b32_e64 v168, v150, v154, s[48:49]
	v_cndmask_b32_e64 v169, v150, v155, s[48:49]
	v_cndmask_b32_e64 v170, v150, v156, s[48:49]
	v_cndmask_b32_e64 v171, v150, v157, s[48:49]
	v_cndmask_b32_e64 v172, v150, v154, s[50:51]
	v_cndmask_b32_e64 v173, v150, v155, s[50:51]
	v_cndmask_b32_e64 v174, v150, v156, s[50:51]
	v_cndmask_b32_e64 v175, v150, v157, s[50:51]
	v_cndmask_b32_e64 v176, v150, v154, s[52:53]
	v_cndmask_b32_e64 v177, v150, v155, s[52:53]
	v_cndmask_b32_e64 v178, v150, v156, s[52:53]
	v_cndmask_b32_e64 v179, v150, v157, s[52:53]
	v_cndmask_b32_e64 v180, v150, v154, s[54:55]
	v_cndmask_b32_e64 v181, v150, v155, s[54:55]
	v_cndmask_b32_e64 v182, v150, v156, s[54:55]
	v_cndmask_b32_e64 v183, v150, v157, s[54:55]
	v_cndmask_b32_e64 v184, v150, v154, s[56:57]
	v_cndmask_b32_e64 v185, v150, v155, s[56:57]
	v_cndmask_b32_e64 v186, v150, v156, s[56:57]
	v_cndmask_b32_e64 v187, v150, v157, s[56:57]
	v_mov_b32_e32 v52, 1
	v_lshlrev_b16_sdwa v52, v52, v78 dst_sel:DWORD dst_unused:UNUSED_PAD src0_sel:DWORD src1_sel:WORD_1
	v_mul_i32_i24_e32 v51, -9, v77
	v_add_u16_e32 v52, v52, v77
	v_mul_u32_u24_e32 v52, 0xa0, v52
	v_add_lshl_u32 v51, v51, v0, 4
	s_waitcnt vmcnt(17)
	v_cndmask_b32_e32 v29, 0, v29, vcc
	v_cndmask_b32_e32 v28, 0, v28, vcc
	v_cndmask_b32_e32 v27, 0, v27, vcc
	v_cndmask_b32_e32 v26, 0, v26, vcc
	v_add3_u32 v51, 0, v52, v51
	ds_write_b128 v51, v[26:29]
	v_lshlrev_b16_e32 v27, 1, v80
	v_mul_i32_i24_e32 v26, -9, v79
	v_add_u16_e32 v27, v27, v79
	v_mul_u32_u24_e32 v27, 0xa0, v27
	v_add_lshl_u32 v26, v26, v62, 4
	s_waitcnt vmcnt(16)
	v_cndmask_b32_e64 v33, 0, v33, s[2:3]
	v_cndmask_b32_e64 v32, 0, v32, s[2:3]
	v_cndmask_b32_e64 v31, 0, v31, s[2:3]
	v_cndmask_b32_e64 v30, 0, v30, s[2:3]
	v_add3_u32 v26, 0, v27, v26
	v_lshlrev_b16_e32 v27, 1, v82
	ds_write_b128 v26, v[30:33]
	v_mul_i32_i24_e32 v26, -9, v81
	v_add_u16_e32 v27, v27, v81
	v_mul_u32_u24_e32 v27, 0xa0, v27
	v_add_lshl_u32 v26, v26, v61, 4
	s_waitcnt vmcnt(15)
	v_cndmask_b32_e64 v37, 0, v37, s[4:5]
	v_cndmask_b32_e64 v36, 0, v36, s[4:5]
	v_cndmask_b32_e64 v35, 0, v35, s[4:5]
	v_cndmask_b32_e64 v34, 0, v34, s[4:5]
	v_add3_u32 v26, 0, v27, v26
	v_lshlrev_b16_e32 v27, 1, v85
	ds_write_b128 v26, v[34:37]
	v_mul_i32_i24_e32 v26, -9, v84
	v_add_u16_e32 v27, v27, v84
	v_mul_u32_u24_e32 v27, 0xa0, v27
	v_add_lshl_u32 v26, v26, v83, 4
	v_mul_u32_u24_e32 v28, 0xca5, v86
	s_waitcnt vmcnt(14)
	v_cndmask_b32_e64 v45, 0, v45, s[8:9]
	v_cndmask_b32_e64 v44, 0, v44, s[8:9]
	v_cndmask_b32_e64 v43, 0, v43, s[8:9]
	v_cndmask_b32_e64 v42, 0, v42, s[8:9]
	v_add3_u32 v26, 0, v27, v26
	v_lshrrev_b32_e32 v28, 18, v28
	ds_write_b128 v26, v[42:45]
	v_mul_u32_u24_e32 v27, 0x1c72, v86
	v_mov_b32_e32 v26, -9
	v_and_b32_e32 v28, 62, v28
	v_mul_i32_i24_sdwa v29, v27, v26 dst_sel:DWORD dst_unused:UNUSED_PAD src0_sel:WORD_1 src1_sel:DWORD
	v_add_u16_sdwa v27, v28, v27 dst_sel:DWORD dst_unused:UNUSED_PAD src0_sel:DWORD src1_sel:WORD_1
	v_mul_u32_u24_e32 v27, 0xa0, v27
	v_add_lshl_u32 v28, v29, v86, 4
	s_movk_i32 s2, 0x164
	v_bfe_u32 v50, v0, 4, 2
	s_waitcnt vmcnt(13)
	v_cndmask_b32_e64 v49, 0, v49, s[10:11]
	v_cndmask_b32_e64 v48, 0, v48, s[10:11]
	v_cndmask_b32_e64 v47, 0, v47, s[10:11]
	v_cndmask_b32_e64 v46, 0, v46, s[10:11]
	v_add3_u32 v27, 0, v27, v28
	v_cmp_gt_u32_e32 vcc, s2, v0
	ds_write_b128 v27, v[46:49]
	s_and_saveexec_b64 s[2:3], vcc
	s_cbranch_execz .LBB2_16
	v_mul_u32_u24_e32 v32, 0xca5, v87
	v_lshrrev_b32_e32 v32, 18, v32
	v_mul_u32_u24_e32 v27, 0x1c72, v87
	v_and_b32_e32 v32, 62, v32
	v_mul_i32_i24_sdwa v26, v27, v26 dst_sel:DWORD dst_unused:UNUSED_PAD src0_sel:WORD_1 src1_sel:DWORD
	v_add_u16_sdwa v27, v32, v27 dst_sel:DWORD dst_unused:UNUSED_PAD src0_sel:DWORD src1_sel:WORD_1
	v_mul_u32_u24_e32 v27, 0xa0, v27
	v_add_lshl_u32 v26, v26, v87, 4
	s_waitcnt vmcnt(12)
	v_cndmask_b32_e64 v31, 0, v41, s[6:7]
	v_cndmask_b32_e64 v30, 0, v40, s[6:7]
	v_cndmask_b32_e64 v29, 0, v39, s[6:7]
	v_cndmask_b32_e64 v28, 0, v38, s[6:7]
	v_add3_u32 v26, 0, v27, v26
	ds_write_b128 v26, v[28:31]
.LBB2_16:
	s_or_b64 exec, exec, s[2:3]
	s_movk_i32 s2, 0x168
	s_waitcnt vmcnt(12)
	v_and_b32_e32 v38, 63, v0
	v_lshlrev_b32_e32 v26, 3, v50
	v_cmp_gt_u32_e32 vcc, s2, v0
	s_and_saveexec_b64 s[2:3], vcc
	s_movk_i32 s4, 0xa0
	v_mad_u32_u24 v27, v0, s4, 0
	v_mov_b32_e32 v28, 0x3c00
	ds_write_b16 v27, v28 offset:144
	s_or_b64 exec, exec, s[2:3]
	v_lshlrev_b32_e32 v39, 2, v50
	v_or_b32_e32 v28, s30, v57
	v_add_u32_e32 v29, v28, v39
	v_sub_u32_e32 v30, v39, v1
	s_movk_i32 s7, 0x80
	v_cmp_gt_u32_e64 s[2:3], 11, v30
	v_cmp_gt_u32_e64 s[4:5], s7, v29
	v_or_b32_e32 v29, 1, v39
	s_and_b64 s[2:3], s[2:3], s[4:5]
	v_mov_b32_e32 v51, 0xff800000
	v_add_u32_e32 v30, v28, v29
	v_sub_u32_e32 v29, v29, v1
	v_cndmask_b32_e64 v52, v51, 0, s[2:3]
	v_cmp_gt_u32_e64 s[2:3], 11, v29
	v_cmp_gt_u32_e64 s[4:5], s7, v30
	v_or_b32_e32 v29, 2, v39
	v_lshrrev_b32_e32 v41, 8, v0
	s_and_b64 s[2:3], s[2:3], s[4:5]
	v_add_u32_e32 v30, v28, v29
	v_sub_u32_e32 v29, v29, v1
	v_cndmask_b32_e64 v53, v51, 0, s[2:3]
	v_cmp_gt_u32_e64 s[2:3], 11, v29
	v_or_b32_e32 v29, 3, v39
	v_mad_u32_u24 v40, v41, 7, v76
	v_cmp_gt_u32_e64 s[4:5], s7, v30
	v_add_u32_e32 v28, v28, v29
	v_mad_u32_u24 v116, v40, 20, v57
	s_and_b64 s[2:3], s[2:3], s[4:5]
	v_cmp_gt_u32_e64 s[4:5], s7, v28
	v_add_u32_e32 v28, v116, v59
	s_movk_i32 s6, 0xa0
	v_mul_lo_u32 v28, v28, s6
	v_add_u32_e32 v117, 0, v28
	v_mul_u32_u24_e32 v27, 7, v41
	v_sub_u32_e32 v29, v29, v1
	v_lshl_add_u32 v112, v26, 1, v117
	s_waitcnt lgkmcnt(0)
	s_barrier
	v_cndmask_b32_e64 v128, v51, 0, s[2:3]
	v_cmp_gt_u32_e64 s[2:3], 11, v29
	ds_read_b128 v[26:29], v112
	s_and_b64 s[2:3], s[2:3], s[4:5]
	ds_read_b128 v[34:37], v112 offset:64
	v_cndmask_b32_e64 v129, v51, 0, s[2:3]
	v_cmp_gt_u32_e32 vcc, 16, v38
	v_add_u32_e32 v116, v116, v39
	s_waitcnt lgkmcnt(1)
	v_mfma_f32_16x16x32_f16 v[30:33], v[26:29], v[10:13], v[160:163]
	ds_read_b128 v[42:45], v117 offset:128
	ds_read_b128 v[46:49], v112 offset:3200
	v_cndmask_b32_e32 v29, 0, v25, vcc
	s_waitcnt lgkmcnt(2)
	v_mfma_f32_16x16x32_f16 v[30:33], v[34:37], v[2:5], v[30:33]
	v_cndmask_b32_e32 v28, 0, v24, vcc
	v_cndmask_b32_e32 v27, 0, v23, vcc
	v_cndmask_b32_e32 v26, 0, v22, vcc
	ds_read_b128 v[34:37], v112 offset:3264
	ds_read_b128 v[76:79], v117 offset:3328
	s_waitcnt lgkmcnt(3)
	v_mfma_f32_16x16x32_f16 v[22:25], v[42:45], v[26:29], v[30:33]
	ds_read_b128 v[42:45], v112 offset:6400
	ds_read_b128 v[80:83], v112 offset:6464
	v_or_b32_e32 v116, v116, v60
	v_mul_lo_u32 v116, v116, s6
	s_waitcnt vmcnt(11)
	v_cvt_pk_f16_f32 v21, v20, v21
	s_waitcnt lgkmcnt(4)
	v_mfma_f32_16x16x32_f16 v[30:33], v[46:49], v[10:13], v[164:167]
	ds_read_b128 v[46:49], v117 offset:6528
	ds_read_b128 v[84:87], v112 offset:9600
	v_cvt_pk_f16_f32 v20, v18, v19
	s_waitcnt lgkmcnt(5)
	v_mfma_f32_16x16x32_f16 v[30:33], v[34:37], v[2:5], v[30:33]
	ds_read_b128 v[88:91], v112 offset:9664
	ds_read_b128 v[92:95], v117 offset:9728
	s_waitcnt lgkmcnt(6)
	v_mfma_f32_16x16x32_f16 v[30:33], v[76:79], v[26:29], v[30:33]
	ds_read_b128 v[76:79], v112 offset:12800
	ds_read_b128 v[96:99], v112 offset:12864
	v_mul_u32_u24_e32 v18, 0xa0, v75
	s_waitcnt lgkmcnt(7)
	v_mfma_f32_16x16x32_f16 v[34:37], v[42:45], v[10:13], v[168:171]
	ds_read_b128 v[42:45], v117 offset:12928
	ds_read_b128 v[100:103], v112 offset:16000
	v_lshlrev_b32_e32 v19, 1, v54
	s_waitcnt lgkmcnt(8)
	v_mfma_f32_16x16x32_f16 v[34:37], v[80:83], v[2:5], v[34:37]
	ds_read_b128 v[80:83], v112 offset:16064
	ds_read_b128 v[104:107], v117 offset:16128
	v_add3_u32 v18, 0, v18, v19
	s_waitcnt lgkmcnt(9)
	v_mfma_f32_16x16x32_f16 v[34:37], v[46:49], v[26:29], v[34:37]
	ds_read_b128 v[108:111], v112 offset:19200
	ds_read_b128 v[112:115], v112 offset:19264
	s_waitcnt lgkmcnt(10)
	v_mfma_f32_16x16x32_f16 v[46:49], v[84:87], v[10:13], v[172:175]
	ds_read_b128 v[84:87], v117 offset:19328
	v_lshlrev_b32_e32 v117, 3, v1
	v_add3_u32 v132, 0, v116, v117
	ds_read_b64_tr_b16 v[118:119], v132 offset:3200
	s_waitcnt lgkmcnt(11)
	v_mfma_f32_16x16x32_f16 v[46:49], v[88:91], v[2:5], v[46:49]
	ds_read_b64_tr_b16 v[116:117], v132
	ds_read_b64_tr_b16 v[88:89], v132 offset:32
	s_waitcnt lgkmcnt(12)
	v_mfma_f32_16x16x32_f16 v[46:49], v[92:95], v[26:29], v[46:49]
	ds_read_b64_tr_b16 v[90:91], v132 offset:3232
	ds_read_b64_tr_b16 v[120:121], v132 offset:64
	s_waitcnt lgkmcnt(13)
	v_mfma_f32_16x16x32_f16 v[76:79], v[76:79], v[10:13], v[176:179]
	ds_read_b64_tr_b16 v[122:123], v132 offset:3264
	s_movk_i32 s8, 0xffee
	s_waitcnt vmcnt(10)
	v_cvt_pk_f16_f32 v17, v16, v17
	ds_read_b64_tr_b16 v[92:93], v132 offset:96
	s_waitcnt lgkmcnt(14)
	v_mfma_f32_16x16x32_f16 v[76:79], v[96:99], v[2:5], v[76:79]
	ds_read_b64_tr_b16 v[94:95], v132 offset:3296
	ds_read_b64_tr_b16 v[96:97], v132 offset:128
	v_cvt_pk_f16_f32 v16, v14, v15
	s_waitcnt lgkmcnt(14)
	v_mfma_f32_16x16x32_f16 v[42:45], v[42:45], v[26:29], v[76:79]
	ds_read_b64_tr_b16 v[98:99], v132 offset:3328
	ds_read_b64_tr_b16 v[124:125], v132 offset:6400
	s_movk_i32 s4, 0x510
	s_nop 0
	v_mfma_f32_16x16x32_f16 v[76:79], v[100:103], v[10:13], v[180:183]
	ds_read_b64_tr_b16 v[126:127], v132 offset:9600
	ds_read_b64_tr_b16 v[100:101], v132 offset:6432
	s_waitcnt lgkmcnt(14)
	v_mfma_f32_16x16x32_f16 v[76:79], v[80:83], v[2:5], v[76:79]
	ds_read_b64_tr_b16 v[102:103], v132 offset:9632
	ds_read_b64_tr_b16 v[80:81], v132 offset:6464
	v_mfma_f32_16x16x32_f16 v[76:79], v[104:107], v[26:29], v[76:79]
	ds_read_b64_tr_b16 v[82:83], v132 offset:9664
	ds_read_b64_tr_b16 v[128:129], v132 offset:6496
	v_mfma_f32_16x16x32_f16 v[10:13], v[108:111], v[10:13], v[184:187]
	s_mov_b32 s2, 0xff800000
	ds_read_b64_tr_b16 v[130:131], v132 offset:9696
	s_movk_i32 s7, 0xe39
	ds_read_b64_tr_b16 v[104:105], v132 offset:6528
	v_mfma_f32_16x16x32_f16 v[2:5], v[112:115], v[2:5], v[10:13]
	ds_read_b64_tr_b16 v[106:107], v132 offset:9728
	s_nop 1
	v_max3_f32 v12, v22, s2, v23
	v_max3_f32 v12, v12, v24, v25
	v_max3_f32 v12, v12, v30, v31
	v_max3_f32 v12, v12, v32, v33
	v_max3_f32 v12, v12, v34, v35
	v_max3_f32 v12, v12, v36, v37
	v_max3_f32 v12, v12, v46, v47
	v_max3_f32 v12, v12, v48, v49
	v_mbcnt_lo_u32_b32 v13, -1, 0
	ds_read_b64_tr_b16 v[10:11], v132 offset:12800
	s_waitcnt lgkmcnt(14)
	v_mfma_f32_16x16x32_f16 v[2:5], v[84:87], v[26:29], v[2:5]
	v_max3_f32 v12, v12, v42, v43
	v_mbcnt_hi_u32_b32 v13, -1, v13
	v_max3_f32 v12, v12, v44, v45
	v_and_b32_e32 v27, 64, v13
	v_max3_f32 v12, v12, v76, v77
	v_xor_b32_e32 v26, 16, v13
	v_add_u32_e32 v27, 64, v27
	v_max3_f32 v12, v12, v78, v79
	v_cmp_lt_i32_e32 vcc, v26, v27
	v_max3_f32 v12, v12, v2, v3
	v_max3_f32 v12, v12, v4, v5
	v_mov_b32_e32 v26, v12
	v_cmp_lt_u32_e64 s[2:3], 15, v38
	s_nop 0
	v_permlane16_swap_b32_e32 v12, v26
	v_cmp_gt_u32_e32 vcc, 11, v40
	s_nop 0
	v_max_f32_e32 v12, v12, v26
	v_mov_b32_e32 v13, v12
	s_nop 1
	v_permlane32_swap_b32_e32 v12, v13
	s_waitcnt lgkmcnt(0)
	s_nop 0
	v_max_f32_e32 v28, v12, v13
	v_sub_f32_e32 v12, v22, v28
	v_sub_f32_e32 v22, v24, v28
	v_sub_f32_e32 v24, v30, v28
	v_sub_f32_e32 v30, v35, v28
	v_exp_f32_e32 v41, v30
	v_sub_f32_e32 v30, v36, v28
	v_exp_f32_e32 v51, v30
	v_sub_f32_e32 v30, v37, v28
	v_exp_f32_e32 v52, v30
	v_sub_f32_e32 v30, v46, v28
	v_exp_f32_e32 v53, v30
	v_sub_f32_e32 v30, v47, v28
	v_exp_f32_e32 v110, v30
	v_sub_f32_e32 v30, v48, v28
	v_sub_f32_e32 v13, v23, v28
	v_sub_f32_e32 v23, v25, v28
	v_sub_f32_e32 v25, v31, v28
	v_exp_f32_e32 v111, v30
	v_sub_f32_e32 v30, v49, v28
	v_exp_f32_e32 v26, v25
	v_sub_f32_e32 v25, v32, v28
	v_sub_f32_e32 v27, v33, v28
	v_exp_f32_e32 v112, v30
	v_sub_f32_e32 v30, v42, v28
	v_exp_f32_e32 v12, v12
	v_exp_f32_e32 v13, v13
	v_exp_f32_e32 v22, v22
	v_exp_f32_e32 v23, v23
	v_exp_f32_e32 v24, v24
	v_exp_f32_e32 v25, v25
	v_exp_f32_e32 v27, v27
	v_exp_f32_e32 v133, v30
	v_sub_f32_e32 v30, v43, v28
	v_exp_f32_e32 v134, v30
	v_sub_f32_e32 v30, v44, v28
	v_exp_f32_e32 v135, v30
	v_sub_f32_e32 v30, v45, v28
	v_sub_f32_e32 v29, v34, v28
	v_exp_f32_e32 v136, v30
	v_sub_f32_e32 v30, v76, v28
	v_exp_f32_e32 v29, v29
	v_exp_f32_e32 v137, v30
	v_sub_f32_e32 v30, v77, v28
	v_cvt_pk_f16_f32 v25, v25, v27
	v_cvt_pk_f16_f32 v24, v24, v26
	v_cvt_pk_f16_f32 v23, v22, v23
	v_cvt_pk_f16_f32 v22, v12, v13
	v_exp_f32_e32 v138, v30
	v_mov_b32_e32 v27, 0xc80
	v_mfma_f32_16x16x32_f16 v[30:33], v[116:119], v[22:25], 0
	ds_read_b64_tr_b16 v[12:13], v132 offset:16000
	ds_read_b64_tr_b16 v[34:35], v132 offset:12832
	v_cndmask_b32_e32 v27, 0, v27, vcc
	v_mfma_f32_16x16x32_f16 v[42:45], v[88:91], v[22:25], 0
	ds_read_b64_tr_b16 v[36:37], v132 offset:16032
	ds_read_b64_tr_b16 v[46:47], v132 offset:12864
	v_sub_f32_e32 v26, v78, v28
	v_mfma_f32_16x16x32_f16 v[84:87], v[120:123], v[22:25], 0
	ds_read_b64_tr_b16 v[48:49], v132 offset:16064
	ds_read_b64_tr_b16 v[88:89], v132 offset:12896
	v_add_u32_e32 v27, v132, v27
	v_mfma_f32_16x16x32_f16 v[92:95], v[92:95], v[22:25], 0
	ds_read_b64_tr_b16 v[90:91], v132 offset:16096
	ds_read_b64_tr_b16 v[108:109], v132 offset:12928
	v_exp_f32_e32 v26, v26
	v_mfma_f32_16x16x32_f16 v[22:25], v[96:99], v[22:25], 0
	v_cvt_pk_f16_f32 v99, v111, v112
	v_cvt_pk_f16_f32 v98, v53, v110
	ds_read_b64_tr_b16 v[110:111], v132 offset:16128
	v_cvt_pk_f16_f32 v97, v51, v52
	v_cvt_pk_f16_f32 v96, v29, v41
	v_sub_f32_e32 v29, v79, v28
	ds_read_b64_tr_b16 v[112:113], v132 offset:19200
	v_mfma_f32_16x16x32_f16 v[30:33], v[124:127], v[96:99], v[30:33]
	ds_read_b64_tr_b16 v[114:115], v27 offset:19200
	ds_read_b64_tr_b16 v[118:119], v27 offset:19232
	v_exp_f32_e32 v29, v29
	v_mfma_f32_16x16x32_f16 v[40:43], v[100:103], v[96:99], v[42:45]
	ds_read_b64_tr_b16 v[116:117], v132 offset:19232
	ds_read_b64_tr_b16 v[76:77], v132 offset:19264
	v_sub_f32_e32 v2, v2, v28
	v_mfma_f32_16x16x32_f16 v[80:83], v[80:83], v[96:99], v[84:87]
	ds_read_b64_tr_b16 v[78:79], v27 offset:19264
	v_cmp_gt_u32_e32 vcc, s4, v61
	s_nop 0
	ds_read_b64_tr_b16 v[84:85], v132 offset:19296
	v_mfma_f32_16x16x32_f16 v[92:95], v[128:131], v[96:99], v[92:95]
	ds_read_b64_tr_b16 v[86:87], v27 offset:19296
	ds_read_b64_tr_b16 v[100:101], v132 offset:19328
	v_mfma_f32_16x16x32_f16 v[22:25], v[104:107], v[96:99], v[22:25]
	ds_read_b64_tr_b16 v[102:103], v27 offset:19328
	ds_write_b64 v18, v[20:21] offset:57600
	v_mul_u32_u24_sdwa v18, v62, s7 dst_sel:DWORD dst_unused:UNUSED_PAD src0_sel:WORD_0 src1_sel:DWORD
	v_mul_i32_i24_sdwa v19, v18, s8 dst_sel:DWORD dst_unused:UNUSED_PAD src0_sel:WORD_1 src1_sel:DWORD
	v_mul_u32_u24_sdwa v14, v18, s6 dst_sel:DWORD dst_unused:UNUSED_PAD src0_sel:WORD_1 src1_sel:DWORD
	v_add_lshl_u32 v15, v19, v62, 3
	v_exp_f32_e32 v18, v2
	v_sub_f32_e32 v19, v3, v28
	v_sub_f32_e32 v2, v4, v28
	v_sub_f32_e32 v21, v5, v28
	v_cvt_pk_f16_f32 v99, v26, v29
	v_cvt_pk_f16_f32 v98, v137, v138
	v_cvt_pk_f16_f32 v97, v135, v136
	v_cvt_pk_f16_f32 v96, v133, v134
	v_add3_u32 v14, 0, v14, v15
	v_exp_f32_e32 v20, v2
	v_exp_f32_e32 v21, v21
	v_exp_f32_e32 v19, v19
	s_waitcnt lgkmcnt(14)
	v_mfma_f32_16x16x32_f16 v[10:13], v[10:13], v[96:99], v[30:33]
	ds_write_b64 v14, v[16:17] offset:57600
	v_mfma_f32_16x16x32_f16 v[14:17], v[34:37], v[96:99], v[40:43]
	v_mfma_f32_16x16x32_f16 v[30:33], v[46:49], v[96:99], v[80:83]
	s_nop 1
	v_mov_b32_e32 v42, 0
	v_cvt_pk_f16_f32 v41, v20, v21
	v_cvt_pk_f16_f32 v40, v18, v19
	s_waitcnt lgkmcnt(14)
	v_mfma_f32_16x16x32_f16 v[2:5], v[88:91], v[96:99], v[92:95]
	v_mov_b32_e32 v43, v42
	s_waitcnt lgkmcnt(12)
	v_mfma_f32_16x16x32_f16 v[34:37], v[108:111], v[96:99], v[22:25]
	s_waitcnt lgkmcnt(10)
	v_mfma_f32_16x16x32_f16 v[22:25], v[112:115], v[40:43], v[10:13]
	s_waitcnt lgkmcnt(8)
	v_mfma_f32_16x16x32_f16 v[18:21], v[116:119], v[40:43], v[14:17]
	s_waitcnt lgkmcnt(6)
	v_mfma_f32_16x16x32_f16 v[14:17], v[76:79], v[40:43], v[30:33]
	s_waitcnt lgkmcnt(4)
	v_mfma_f32_16x16x32_f16 v[10:13], v[84:87], v[40:43], v[2:5]
	s_waitcnt lgkmcnt(2)
	v_mfma_f32_16x16x32_f16 v[2:5], v[100:103], v[40:43], v[34:37]
	s_and_saveexec_b64 s[4:5], vcc
	s_cbranch_execz .LBB2_20
	v_mul_u32_u24_sdwa v26, v61, s7 dst_sel:DWORD dst_unused:UNUSED_PAD src0_sel:WORD_0 src1_sel:DWORD
	v_mul_i32_i24_sdwa v27, v26, s8 dst_sel:DWORD dst_unused:UNUSED_PAD src0_sel:WORD_1 src1_sel:DWORD
	s_waitcnt vmcnt(8)
	v_cvt_pk_f16_f32 v9, v8, v9
	v_cvt_pk_f16_f32 v8, v6, v7
	v_mul_u32_u24_sdwa v6, v26, s6 dst_sel:DWORD dst_unused:UNUSED_PAD src0_sel:WORD_1 src1_sel:DWORD
	v_add_lshl_u32 v7, v27, v61, 3
	v_add3_u32 v6, 0, v6, v7
	ds_write_b64 v6, v[8:9] offset:57600

	.amdhsa_kernel _Z5k_ncaILi1EEvPKDF16_S1_PKfS3_PDF16_S3_S3_S3_S3_Pf
		.amdhsa_group_segment_fixed_size 0
		.amdhsa_private_segment_fixed_size 0
		.amdhsa_kernarg_size 80
		.amdhsa_user_sgpr_count 2
		.amdhsa_user_sgpr_dispatch_ptr 0
		.amdhsa_user_sgpr_queue_ptr 0
		.amdhsa_user_sgpr_kernarg_segment_ptr 1
		.amdhsa_user_sgpr_dispatch_id 0
		.amdhsa_user_sgpr_kernarg_preload_length 0
		.amdhsa_user_sgpr_kernarg_preload_offset 0
		.amdhsa_user_sgpr_private_segment_size 0
		.amdhsa_uses_dynamic_stack 0
		.amdhsa_enable_private_segment 0
		.amdhsa_system_sgpr_workgroup_id_x 1
		.amdhsa_system_sgpr_workgroup_id_y 0
		.amdhsa_system_sgpr_workgroup_id_z 0
		.amdhsa_system_sgpr_workgroup_info 0
		.amdhsa_system_vgpr_workitem_id 0
		.amdhsa_next_free_vgpr 192
		.amdhsa_next_free_sgpr 96
		.amdhsa_accum_offset 192
		.amdhsa_reserve_vcc 1
		.amdhsa_float_round_mode_32 0
		.amdhsa_float_round_mode_16_64 0
		.amdhsa_float_denorm_mode_32 3
		.amdhsa_float_denorm_mode_16_64 3
		.amdhsa_dx10_clamp 1
		.amdhsa_ieee_mode 1
		.amdhsa_fp16_overflow 0
		.amdhsa_tg_split 0
		.amdhsa_exception_fp_ieee_invalid_op 0
		.amdhsa_exception_fp_denorm_src 0
		.amdhsa_exception_fp_ieee_div_zero 0
		.amdhsa_exception_fp_ieee_overflow 0
		.amdhsa_exception_fp_ieee_underflow 0
		.amdhsa_exception_fp_ieee_inexact 0
		.amdhsa_exception_int_div_zero 0
	.end_amdhsa_kernel
